# v76 + removed the compiler's conservative alias s_waitcnt vmcnt(0) before the V-fragment LDS reads in the 5 attention tile loops (next-tile K/V LDS-DMA now overlaps PV; waited at loop top)
# speedup vs baseline: 1.0099x; 1.0099x over previous
.LBB0_3630:
	v_exp_f32_e32 v0, v34
	v_exp_f32_e32 v90, v50
	v_exp_f32_e32 v91, v35
	v_exp_f32_e32 v92, v51
	v_exp_f32_e32 v93, v36
	v_exp_f32_e32 v94, v52
	v_exp_f32_e32 v95, v37
	v_exp_f32_e32 v96, v53
	v_add_f32_e32 v34, 0, v0
	v_add_f32_e32 v50, 0, v90
	v_add_f32_e32 v34, v91, v34
	v_add_f32_e32 v35, v92, v50
	v_add_f32_e32 v34, v93, v34
	v_add_f32_e32 v36, v94, v35
	v_add_f32_e32 v35, v95, v34
	v_add_f32_e32 v34, v96, v36
	v_exp_f32_e32 v37, v38
	v_exp_f32_e32 v36, v54
	v_exp_f32_e32 v39, v39
	v_exp_f32_e32 v38, v55
	v_exp_f32_e32 v51, v40
	v_exp_f32_e32 v50, v56
	v_exp_f32_e32 v41, v41
	v_exp_f32_e32 v40, v57
	v_exp_f32_e32 v53, v42
	v_exp_f32_e32 v52, v58
	v_pk_add_f32 v[34:35], v[36:37], v[34:35]
	v_exp_f32_e32 v55, v43
	v_exp_f32_e32 v54, v59
	v_pk_add_f32 v[34:35], v[38:39], v[34:35]
	v_exp_f32_e32 v57, v44
	v_exp_f32_e32 v56, v60
	v_pk_add_f32 v[34:35], v[50:51], v[34:35]
	v_exp_f32_e32 v59, v45
	v_exp_f32_e32 v58, v61
	v_pk_add_f32 v[34:35], v[40:41], v[34:35]
	v_exp_f32_e32 v61, v46
	v_exp_f32_e32 v60, v62
	v_pk_add_f32 v[34:35], v[52:53], v[34:35]
	v_exp_f32_e32 v87, v47
	v_exp_f32_e32 v86, v63
	v_pk_add_f32 v[34:35], v[54:55], v[34:35]
	v_exp_f32_e32 v63, v48
	v_exp_f32_e32 v62, v64
	v_exp_f32_e32 v89, v49
	v_exp_f32_e32 v88, v65
	v_pk_add_f32 v[34:35], v[56:57], v[34:35]
	v_cvt_pk_bf16_f32 v46, v0, v91
	v_pk_add_f32 v[34:35], v[58:59], v[34:35]
	v_add_u32_e32 v0, s0, v125
	v_pk_add_f32 v[34:35], v[60:61], v[34:35]
	v_add3_u32 v0, v0, v126, v122
	v_pk_add_f32 v[34:35], v[86:87], v[34:35]
	v_cvt_pk_bf16_f32 v49, v51, v41
	v_pk_add_f32 v[34:35], v[62:63], v[34:35]
	v_cvt_pk_bf16_f32 v45, v63, v89
	v_cvt_pk_bf16_f32 v41, v62, v88
	ds_read_b64_tr_b16 v[62:63], v0 offset:16384
	ds_read_b64_tr_b16 v[64:65], v0 offset:16896
	v_pk_add_f32 v[34:35], v[88:89], v[34:35]
	v_cvt_pk_bf16_f32 v47, v93, v95
	v_add_f32_e32 v34, v34, v35
	v_cvt_pk_bf16_f32 v48, v37, v39
	v_cvt_pk_bf16_f32 v44, v61, v87
	v_cvt_pk_bf16_f32 v37, v50, v40
	v_cvt_pk_bf16_f32 v40, v60, v86
	ds_read_b64_tr_b16 v[86:87], v0 offset:17408
	ds_read_b64_tr_b16 v[88:89], v0 offset:17920
	v_add_f32_e32 v120, v120, v34
	v_cvt_pk_bf16_f32 v34, v90, v92
	ds_read_b64_tr_b16 v[90:91], v0 offset:18432
	ds_read_b64_tr_b16 v[92:93], v0 offset:18944
	s_waitcnt lgkmcnt(4)
	v_mfma_f32_32x32x16_bf16 v[2:17], v[62:65], v[46:49], v[2:17]
	v_cvt_pk_bf16_f32 v42, v53, v55
	v_cvt_pk_bf16_f32 v43, v57, v59
	v_cvt_pk_bf16_f32 v35, v94, v96
	ds_read_b64_tr_b16 v[94:95], v0 offset:19456
	ds_read_b64_tr_b16 v[96:97], v0 offset:19968
	v_cvt_pk_bf16_f32 v36, v36, v38
	v_cvt_pk_bf16_f32 v38, v52, v54
	s_waitcnt lgkmcnt(4)
	v_mfma_f32_32x32x16_bf16 v[2:17], v[86:89], v[42:45], v[2:17]
	ds_read_b64_tr_b16 v[98:99], v0 offset:20480
	ds_read_b64_tr_b16 v[100:101], v0 offset:20992
	v_cvt_pk_bf16_f32 v39, v56, v58
	s_xor_b32 s2, s2, 1
	s_cmp_lt_i32 s47, 0
	s_waitcnt lgkmcnt(4)
	v_mfma_f32_32x32x16_bf16 v[2:17], v[90:93], v[34:37], v[2:17]
	ds_read_b64_tr_b16 v[58:59], v0 offset:21504
	ds_read_b64_tr_b16 v[60:61], v0 offset:22016
	s_waitcnt lgkmcnt(4)
	v_mfma_f32_32x32x16_bf16 v[2:17], v[94:97], v[38:41], v[2:17]
	ds_read_b64_tr_b16 v[50:51], v0 offset:22528
	ds_read_b64_tr_b16 v[52:53], v0 offset:23040
	s_waitcnt lgkmcnt(4)
	v_mfma_f32_32x32x16_bf16 v[18:33], v[98:101], v[46:49], v[18:33]
	ds_read_b64_tr_b16 v[54:55], v0 offset:23552
	ds_read_b64_tr_b16 v[56:57], v0 offset:24064
	s_waitcnt lgkmcnt(4)
	v_mfma_f32_32x32x16_bf16 v[18:33], v[58:61], v[42:45], v[18:33]
	s_waitcnt lgkmcnt(2)
	v_mfma_f32_32x32x16_bf16 v[18:33], v[50:53], v[34:37], v[18:33]
	s_waitcnt lgkmcnt(0)
	v_mfma_f32_32x32x16_bf16 v[18:33], v[54:57], v[38:41], v[18:33]
	s_cbranch_scc1 .LBB0_3633
	s_mov_b32 s8, s47
	v_mov_b32_e32 v86, v2
	v_mov_b32_e32 v87, v3
	v_mov_b32_e32 v88, v4
	v_mov_b32_e32 v89, v5
	v_mov_b32_e32 v90, v6
	v_mov_b32_e32 v91, v7
	v_mov_b32_e32 v92, v8
	v_mov_b32_e32 v93, v9
	v_mov_b32_e32 v94, v10
	v_mov_b32_e32 v95, v11
	v_mov_b32_e32 v96, v12
	v_mov_b32_e32 v97, v13
	v_mov_b32_e32 v98, v14
	v_mov_b32_e32 v99, v15
	v_mov_b32_e32 v100, v16
	v_mov_b32_e32 v101, v17
	v_mov_b32_e32 v102, v18
	v_mov_b32_e32 v103, v19
	v_mov_b32_e32 v104, v20
	v_mov_b32_e32 v105, v21
	v_mov_b32_e32 v106, v22
	v_mov_b32_e32 v107, v23
	v_mov_b32_e32 v108, v24
	v_mov_b32_e32 v109, v25
	v_mov_b32_e32 v110, v26
	v_mov_b32_e32 v111, v27
	v_mov_b32_e32 v112, v28
	v_mov_b32_e32 v113, v29
	v_mov_b32_e32 v114, v30
	v_mov_b32_e32 v115, v31
	v_mov_b32_e32 v116, v32
	v_mov_b32_e32 v117, v33
	s_branch .LBB0_3619

.LBB0_3648:
	v_add_u32_e32 v8, s55, v138
	v_add3_u32 v161, v8, v139, v135
	v_exp_f32_e32 v141, v96
	v_exp_f32_e32 v157, v98
	v_exp_f32_e32 v96, v84
	v_exp_f32_e32 v98, v85
	v_exp_f32_e32 v2, v86
	v_exp_f32_e32 v6, v87
	ds_read_b64_tr_b16 v[84:85], v161 offset:16384
	ds_read_b64_tr_b16 v[86:87], v161 offset:16896
	v_exp_f32_e32 v155, v97
	v_exp_f32_e32 v159, v99
	v_exp_f32_e32 v97, v100
	v_exp_f32_e32 v99, v101
	v_exp_f32_e32 v3, v102
	v_exp_f32_e32 v7, v103
	v_exp_f32_e32 v146, v80
	v_exp_f32_e32 v10, v88
	v_exp_f32_e32 v12, v89
	v_exp_f32_e32 v14, v90
	v_exp_f32_e32 v80, v91
	v_cvt_pk_bf16_f32 v88, v141, v155
	v_cvt_pk_bf16_f32 v89, v157, v159
	v_cvt_pk_bf16_f32 v90, v97, v99
	v_cvt_pk_bf16_f32 v91, v3, v7
	ds_read_b64_tr_b16 v[100:101], v161 offset:17408
	ds_read_b64_tr_b16 v[102:103], v161 offset:17920
	v_exp_f32_e32 v156, v81
	v_exp_f32_e32 v11, v104
	v_exp_f32_e32 v13, v105
	v_exp_f32_e32 v15, v106
	v_exp_f32_e32 v81, v107
	ds_read_b64_tr_b16 v[104:105], v161 offset:18432
	ds_read_b64_tr_b16 v[106:107], v161 offset:18944
	s_waitcnt lgkmcnt(4)
	v_mfma_f32_32x32x16_bf16 v[64:79], v[84:87], v[88:91], v[64:79]
	v_exp_f32_e32 v160, v83
	v_exp_f32_e32 v83, v108
	v_exp_f32_e32 v5, v109
	v_exp_f32_e32 v9, v110
	v_exp_f32_e32 v151, v111
	v_cvt_pk_bf16_f32 v84, v11, v13
	v_cvt_pk_bf16_f32 v85, v15, v81
	v_cvt_pk_bf16_f32 v86, v83, v5
	v_cvt_pk_bf16_f32 v87, v9, v151
	ds_read_b64_tr_b16 v[108:109], v161 offset:19456
	ds_read_b64_tr_b16 v[110:111], v161 offset:19968
	s_waitcnt lgkmcnt(4)
	v_mfma_f32_32x32x16_bf16 v[64:79], v[100:103], v[84:87], v[64:79]
	v_exp_f32_e32 v158, v82
	v_cvt_pk_bf16_f32 v100, v146, v156
	v_cvt_pk_bf16_f32 v102, v96, v98
	v_cvt_pk_bf16_f32 v103, v2, v6
	v_cvt_pk_bf16_f32 v101, v158, v160
	ds_read_b64_tr_b16 v[142:143], v161 offset:20480
	ds_read_b64_tr_b16 v[144:145], v161 offset:20992
	s_waitcnt lgkmcnt(4)
	v_mfma_f32_32x32x16_bf16 v[64:79], v[104:107], v[100:103], v[64:79]
	v_exp_f32_e32 v82, v92
	v_exp_f32_e32 v4, v93
	v_exp_f32_e32 v8, v94
	v_exp_f32_e32 v150, v95
	v_cvt_pk_bf16_f32 v92, v10, v12
	v_cvt_pk_bf16_f32 v93, v14, v80
	v_cvt_pk_bf16_f32 v94, v82, v4
	v_cvt_pk_bf16_f32 v95, v8, v150
	ds_read_b64_tr_b16 v[104:105], v161 offset:21504
	ds_read_b64_tr_b16 v[106:107], v161 offset:22016
	s_waitcnt lgkmcnt(4)
	v_mfma_f32_32x32x16_bf16 v[64:79], v[108:111], v[92:95], v[64:79]
	ds_read_b64_tr_b16 v[108:109], v161 offset:22528
	ds_read_b64_tr_b16 v[110:111], v161 offset:23040
	s_xor_b32 s53, s53, 1
	s_cmp_gt_i32 s54, -1
	s_waitcnt lgkmcnt(4)
	v_mfma_f32_32x32x16_bf16 v[48:63], v[142:145], v[88:91], v[48:63]
	ds_read_b64_tr_b16 v[142:143], v161 offset:23552
	ds_read_b64_tr_b16 v[144:145], v161 offset:24064
	s_waitcnt lgkmcnt(4)
	v_mfma_f32_32x32x16_bf16 v[48:63], v[104:107], v[84:87], v[48:63]
	ds_read_b64_tr_b16 v[104:105], v161 offset:24576
	ds_read_b64_tr_b16 v[106:107], v161 offset:25088
	s_waitcnt lgkmcnt(4)
	v_mfma_f32_32x32x16_bf16 v[48:63], v[108:111], v[100:103], v[48:63]
	ds_read_b64_tr_b16 v[108:109], v161 offset:25600
	ds_read_b64_tr_b16 v[110:111], v161 offset:26112
	s_waitcnt lgkmcnt(4)
	v_mfma_f32_32x32x16_bf16 v[48:63], v[142:145], v[92:95], v[48:63]
	ds_read_b64_tr_b16 v[142:143], v161 offset:26624
	ds_read_b64_tr_b16 v[144:145], v161 offset:27136
	s_waitcnt lgkmcnt(4)
	v_mfma_f32_32x32x16_bf16 v[32:47], v[104:107], v[88:91], v[32:47]
	ds_read_b64_tr_b16 v[104:105], v161 offset:27648
	ds_read_b64_tr_b16 v[106:107], v161 offset:28160
	s_waitcnt lgkmcnt(4)
	v_mfma_f32_32x32x16_bf16 v[32:47], v[108:111], v[84:87], v[32:47]
	ds_read_b64_tr_b16 v[108:109], v161 offset:28672
	ds_read_b64_tr_b16 v[110:111], v161 offset:29184
	s_waitcnt lgkmcnt(4)
	v_mfma_f32_32x32x16_bf16 v[32:47], v[142:145], v[100:103], v[32:47]
	ds_read_b64_tr_b16 v[142:143], v161 offset:29696
	ds_read_b64_tr_b16 v[144:145], v161 offset:30208
	s_waitcnt lgkmcnt(4)
	v_mfma_f32_32x32x16_bf16 v[32:47], v[104:107], v[92:95], v[32:47]
	v_add_f32_e32 v104, 0, v141
	v_add_f32_e32 v105, 0, v146
	v_add_f32_e32 v104, v155, v104
	v_add_f32_e32 v141, v156, v105
	v_add_f32_e32 v146, v157, v104
	ds_read_b64_tr_b16 v[104:105], v161 offset:30720
	ds_read_b64_tr_b16 v[106:107], v161 offset:31232
	s_waitcnt lgkmcnt(4)
	v_mfma_f32_32x32x16_bf16 v[16:31], v[108:111], v[88:91], v[16:31]
	v_add_f32_e32 v88, v158, v141
	v_add_f32_e32 v89, v159, v146
	v_add_f32_e32 v88, v160, v88
	v_add_f32_e64 v88, v96, v88
	v_add_f32_e64 v89, v97, v89
	ds_read_b64_tr_b16 v[90:91], v161 offset:32256
	v_pk_add_f32 v[96:97], v[98:99], v[88:89]
	ds_read_b64_tr_b16 v[88:89], v161 offset:31744
	s_waitcnt lgkmcnt(4)
	v_mfma_f32_32x32x16_bf16 v[16:31], v[142:145], v[84:87], v[16:31]
	v_add_f32_e64 v2, v2, v96
	v_add_f32_e64 v3, v3, v97
	v_add_f32_e64 v2, v6, v2
	v_add_f32_e64 v3, v7, v3
	v_add_f32_e64 v2, v10, v2
	v_add_f32_e64 v3, v11, v3
	s_waitcnt lgkmcnt(2)
	v_mfma_f32_32x32x16_bf16 v[16:31], v[104:107], v[100:103], v[16:31]
	v_add_f32_e64 v2, v12, v2
	v_add_f32_e64 v3, v13, v3
	v_add_f32_e64 v2, v14, v2
	v_add_f32_e64 v3, v15, v3
	v_add_f32_e64 v2, v80, v2
	v_add_f32_e64 v3, v81, v3
	v_pk_add_f32 v[2:3], v[82:83], v[2:3]
	s_waitcnt lgkmcnt(0)
	v_mfma_f32_32x32x16_bf16 v[16:31], v[88:91], v[92:95], v[16:31]
	v_add_f32_e64 v2, v4, v2
	v_add_f32_e64 v3, v5, v3
	v_add_f32_e64 v2, v8, v2
	v_add_f32_e64 v3, v9, v3
	v_add_f32_e64 v2, v150, v2
	v_add_f32_e64 v3, v151, v3
	v_add_f32_e32 v2, v2, v3
	v_add_f32_e32 v140, v140, v2
	s_cbranch_scc0 .LBB0_3651
	s_mov_b32 s6, s54
	s_branch .LBB0_3637

.LBB0_3746:
	v_exp_f32_e32 v144, v66
	v_exp_f32_e32 v66, v72
	v_add_u32_e32 v72, s92, v158
	v_add3_u32 v184, v72, v159, v157
	v_exp_f32_e32 v150, v83
	v_exp_f32_e32 v151, v67
	v_exp_f32_e32 v182, v85
	v_exp_f32_e32 v108, v71
	v_exp_f32_e32 v67, v88
	v_exp_f32_e32 v71, v89
	v_exp_f32_e32 v83, v90
	v_exp_f32_e32 v85, v91
	ds_read_b64_tr_b16 v[88:89], v184 offset:16384
	ds_read_b64_tr_b16 v[90:91], v184 offset:16896
	v_exp_f32_e32 v111, v82
	v_exp_f32_e32 v180, v84
	v_exp_f32_e32 v107, v86
	v_exp_f32_e32 v109, v87
	v_exp_f32_e32 v183, v69
	v_exp_f32_e32 v84, v75
	v_exp_f32_e32 v75, v92
	v_exp_f32_e32 v87, v93
	v_exp_f32_e32 v86, v77
	v_exp_f32_e32 v77, v94
	v_exp_f32_e32 v69, v95
	v_cvt_pk_bf16_f32 v92, v111, v150
	v_cvt_pk_bf16_f32 v93, v180, v182
	v_cvt_pk_bf16_f32 v94, v107, v109
	v_cvt_pk_bf16_f32 v95, v67, v71
	ds_read_b64_tr_b16 v[164:165], v184 offset:17408
	ds_read_b64_tr_b16 v[166:167], v184 offset:17920
	ds_read_b64_tr_b16 v[168:169], v184 offset:18432
	ds_read_b64_tr_b16 v[170:171], v184 offset:18944
	s_waitcnt lgkmcnt(4)
	v_mfma_f32_32x32x16_bf16 v[50:65], v[88:91], v[92:95], v[50:65]
	v_exp_f32_e32 v106, v70
	v_exp_f32_e32 v70, v73
	v_exp_f32_e32 v73, v96
	v_exp_f32_e32 v97, v97
	v_cvt_pk_bf16_f32 v88, v83, v85
	v_cvt_pk_bf16_f32 v89, v75, v87
	v_cvt_pk_bf16_f32 v90, v77, v69
	v_cvt_pk_bf16_f32 v91, v73, v97
	ds_read_b64_tr_b16 v[172:173], v184 offset:19456
	ds_read_b64_tr_b16 v[174:175], v184 offset:19968
	s_waitcnt lgkmcnt(4)
	v_mfma_f32_32x32x16_bf16 v[50:65], v[164:167], v[88:91], v[50:65]
	v_exp_f32_e32 v181, v68
	v_cvt_pk_bf16_f32 v164, v144, v151
	v_cvt_pk_bf16_f32 v166, v106, v108
	v_cvt_pk_bf16_f32 v167, v66, v70
	v_cvt_pk_bf16_f32 v165, v181, v183
	ds_read_b64_tr_b16 v[176:177], v184 offset:20480
	ds_read_b64_tr_b16 v[178:179], v184 offset:20992
	s_waitcnt lgkmcnt(4)
	v_mfma_f32_32x32x16_bf16 v[50:65], v[168:171], v[164:167], v[50:65]
	v_exp_f32_e32 v82, v74
	v_exp_f32_e32 v74, v76
	v_exp_f32_e32 v76, v78
	v_exp_f32_e32 v68, v79
	v_exp_f32_e32 v72, v80
	v_exp_f32_e32 v96, v81
	v_cvt_pk_bf16_f32 v78, v82, v84
	v_cvt_pk_bf16_f32 v79, v74, v86
	v_cvt_pk_bf16_f32 v80, v76, v68
	v_cvt_pk_bf16_f32 v81, v72, v96
	ds_read_b64_tr_b16 v[168:169], v184 offset:21504
	ds_read_b64_tr_b16 v[170:171], v184 offset:22016
	s_waitcnt lgkmcnt(4)
	v_mfma_f32_32x32x16_bf16 v[50:65], v[172:175], v[78:81], v[50:65]
	ds_read_b64_tr_b16 v[172:173], v184 offset:22528
	ds_read_b64_tr_b16 v[174:175], v184 offset:23040
	v_add_f32_e32 v111, 0, v111
	v_add_f32_e32 v144, 0, v144
	v_add_f32_e32 v111, v150, v111
	v_add_f32_e32 v144, v151, v144
	v_add_f32_e32 v111, v180, v111
	s_waitcnt lgkmcnt(4)
	v_mfma_f32_32x32x16_bf16 v[34:49], v[176:179], v[92:95], v[34:49]
	ds_read_b64_tr_b16 v[176:177], v184 offset:23552
	ds_read_b64_tr_b16 v[178:179], v184 offset:24064
	s_xor_b32 s0, s0, 1
	s_cmp_gt_i32 s85, -1
	s_waitcnt lgkmcnt(4)
	v_mfma_f32_32x32x16_bf16 v[34:49], v[168:171], v[88:91], v[34:49]
	ds_read_b64_tr_b16 v[168:169], v184 offset:24576
	ds_read_b64_tr_b16 v[170:171], v184 offset:25088
	s_waitcnt lgkmcnt(4)
	v_mfma_f32_32x32x16_bf16 v[34:49], v[172:175], v[164:167], v[34:49]
	ds_read_b64_tr_b16 v[172:173], v184 offset:25600
	ds_read_b64_tr_b16 v[174:175], v184 offset:26112
	s_waitcnt lgkmcnt(4)
	v_mfma_f32_32x32x16_bf16 v[34:49], v[176:179], v[78:81], v[34:49]
	ds_read_b64_tr_b16 v[176:177], v184 offset:26624
	ds_read_b64_tr_b16 v[178:179], v184 offset:27136
	s_waitcnt lgkmcnt(4)
	v_mfma_f32_32x32x16_bf16 v[18:33], v[168:171], v[92:95], v[18:33]
	ds_read_b64_tr_b16 v[168:169], v184 offset:27648
	ds_read_b64_tr_b16 v[170:171], v184 offset:28160
	s_waitcnt lgkmcnt(4)
	v_mfma_f32_32x32x16_bf16 v[18:33], v[172:175], v[88:91], v[18:33]
	ds_read_b64_tr_b16 v[172:173], v184 offset:28672
	ds_read_b64_tr_b16 v[174:175], v184 offset:29184
	s_waitcnt lgkmcnt(4)
	v_mfma_f32_32x32x16_bf16 v[18:33], v[176:179], v[164:167], v[18:33]
	ds_read_b64_tr_b16 v[176:177], v184 offset:29696
	ds_read_b64_tr_b16 v[178:179], v184 offset:30208
	s_waitcnt lgkmcnt(4)
	v_mfma_f32_32x32x16_bf16 v[18:33], v[168:171], v[78:81], v[18:33]
	ds_read_b64_tr_b16 v[168:169], v184 offset:30720
	ds_read_b64_tr_b16 v[170:171], v184 offset:31232
	s_waitcnt lgkmcnt(4)
	v_mfma_f32_32x32x16_bf16 v[2:17], v[172:175], v[92:95], v[2:17]
	v_add_f32_e32 v92, v181, v144
	v_add_f32_e32 v93, v182, v111
	v_add_f32_e32 v92, v183, v92
	v_add_f32_e64 v92, v106, v92
	v_add_f32_e64 v93, v107, v93
	ds_read_b64_tr_b16 v[94:95], v184 offset:32256
	v_pk_add_f32 v[106:107], v[108:109], v[92:93]
	ds_read_b64_tr_b16 v[92:93], v184 offset:31744
	s_waitcnt lgkmcnt(4)
	v_mfma_f32_32x32x16_bf16 v[2:17], v[176:179], v[88:91], v[2:17]
	v_add_f32_e64 v66, v66, v106
	v_add_f32_e64 v67, v67, v107
	v_add_f32_e64 v66, v70, v66
	v_add_f32_e64 v67, v71, v67
	v_add_f32_e64 v66, v82, v66
	v_add_f32_e64 v67, v83, v67
	s_waitcnt lgkmcnt(2)
	v_mfma_f32_32x32x16_bf16 v[2:17], v[168:171], v[164:167], v[2:17]
	v_add_f32_e64 v66, v84, v66
	v_add_f32_e64 v67, v85, v67
	v_add_f32_e64 v66, v74, v66
	v_add_f32_e64 v67, v75, v67
	v_add_f32_e64 v66, v86, v66
	v_add_f32_e64 v67, v87, v67
	v_pk_add_f32 v[66:67], v[76:77], v[66:67]
	s_waitcnt lgkmcnt(0)
	v_mfma_f32_32x32x16_bf16 v[2:17], v[92:95], v[78:81], v[2:17]
	v_add_f32_e64 v66, v68, v66
	v_add_f32_e64 v67, v69, v67
	v_add_f32_e64 v66, v72, v66
	v_add_f32_e64 v67, v73, v67
	v_add_f32_e64 v66, v96, v66
	v_add_f32_e64 v67, v97, v67
	v_add_f32_e32 v66, v66, v67
	v_add_f32_e32 v99, v99, v66
	s_cbranch_scc0 .LBB0_3749
	s_mov_b32 s8, s85
	s_branch .LBB0_3733

.LBB0_3769:
	v_add_u32_e32 v8, s42, v158
	v_add3_u32 v179, v8, v159, v157
	v_exp_f32_e32 v0, v96
	v_exp_f32_e32 v175, v98
	v_exp_f32_e32 v96, v84
	v_exp_f32_e32 v98, v85
	v_exp_f32_e32 v2, v86
	v_exp_f32_e32 v6, v87
	ds_read_b64_tr_b16 v[84:85], v179 offset:16384
	ds_read_b64_tr_b16 v[86:87], v179 offset:16896
	v_exp_f32_e32 v173, v97
	v_exp_f32_e32 v177, v99
	v_exp_f32_e32 v97, v100
	v_exp_f32_e32 v99, v101
	v_exp_f32_e32 v3, v102
	v_exp_f32_e32 v7, v103
	v_exp_f32_e32 v172, v80
	v_exp_f32_e32 v10, v88
	v_exp_f32_e32 v12, v89
	v_exp_f32_e32 v14, v90
	v_exp_f32_e32 v80, v91
	v_cvt_pk_bf16_f32 v88, v0, v173
	v_cvt_pk_bf16_f32 v89, v175, v177
	v_cvt_pk_bf16_f32 v90, v97, v99
	v_cvt_pk_bf16_f32 v91, v3, v7
	ds_read_b64_tr_b16 v[100:101], v179 offset:17408
	ds_read_b64_tr_b16 v[102:103], v179 offset:17920
	v_exp_f32_e32 v174, v81
	v_exp_f32_e32 v11, v104
	v_exp_f32_e32 v13, v105
	v_exp_f32_e32 v15, v106
	v_exp_f32_e32 v81, v107
	ds_read_b64_tr_b16 v[104:105], v179 offset:18432
	ds_read_b64_tr_b16 v[106:107], v179 offset:18944
	s_waitcnt lgkmcnt(4)
	v_mfma_f32_32x32x16_bf16 v[64:79], v[84:87], v[88:91], v[64:79]
	v_exp_f32_e32 v178, v83
	v_exp_f32_e32 v83, v108
	v_exp_f32_e32 v5, v109
	v_exp_f32_e32 v9, v110
	v_exp_f32_e32 v171, v111
	v_cvt_pk_bf16_f32 v84, v11, v13
	v_cvt_pk_bf16_f32 v85, v15, v81
	v_cvt_pk_bf16_f32 v86, v83, v5
	v_cvt_pk_bf16_f32 v87, v9, v171
	ds_read_b64_tr_b16 v[108:109], v179 offset:19456
	ds_read_b64_tr_b16 v[110:111], v179 offset:19968
	s_waitcnt lgkmcnt(4)
	v_mfma_f32_32x32x16_bf16 v[64:79], v[100:103], v[84:87], v[64:79]
	v_exp_f32_e32 v176, v82
	v_cvt_pk_bf16_f32 v100, v172, v174
	v_cvt_pk_bf16_f32 v102, v96, v98
	v_cvt_pk_bf16_f32 v103, v2, v6
	v_cvt_pk_bf16_f32 v101, v176, v178
	ds_read_b64_tr_b16 v[166:167], v179 offset:20480
	ds_read_b64_tr_b16 v[168:169], v179 offset:20992
	s_waitcnt lgkmcnt(4)
	v_mfma_f32_32x32x16_bf16 v[64:79], v[104:107], v[100:103], v[64:79]
	v_exp_f32_e32 v82, v92
	v_exp_f32_e32 v4, v93
	v_exp_f32_e32 v8, v94
	v_exp_f32_e32 v170, v95
	v_cvt_pk_bf16_f32 v92, v10, v12
	v_cvt_pk_bf16_f32 v93, v14, v80
	v_cvt_pk_bf16_f32 v94, v82, v4
	v_cvt_pk_bf16_f32 v95, v8, v170
	ds_read_b64_tr_b16 v[104:105], v179 offset:21504
	ds_read_b64_tr_b16 v[106:107], v179 offset:22016
	s_waitcnt lgkmcnt(4)
	v_mfma_f32_32x32x16_bf16 v[64:79], v[108:111], v[92:95], v[64:79]
	ds_read_b64_tr_b16 v[108:109], v179 offset:22528
	ds_read_b64_tr_b16 v[110:111], v179 offset:23040
	v_add_f32_e32 v0, 0, v0
	v_add_f32_e32 v0, v173, v0
	v_add_f32_e32 v0, v175, v0
	s_xor_b32 s2, s2, 1
	s_cmp_lt_i32 s3, 0
	s_waitcnt lgkmcnt(4)
	v_mfma_f32_32x32x16_bf16 v[48:63], v[166:169], v[88:91], v[48:63]
	ds_read_b64_tr_b16 v[166:167], v179 offset:23552
	ds_read_b64_tr_b16 v[168:169], v179 offset:24064
	s_waitcnt lgkmcnt(4)
	v_mfma_f32_32x32x16_bf16 v[48:63], v[104:107], v[84:87], v[48:63]
	ds_read_b64_tr_b16 v[104:105], v179 offset:24576
	ds_read_b64_tr_b16 v[106:107], v179 offset:25088
	s_waitcnt lgkmcnt(4)
	v_mfma_f32_32x32x16_bf16 v[48:63], v[108:111], v[100:103], v[48:63]
	ds_read_b64_tr_b16 v[108:109], v179 offset:25600
	ds_read_b64_tr_b16 v[110:111], v179 offset:26112
	s_waitcnt lgkmcnt(4)
	v_mfma_f32_32x32x16_bf16 v[48:63], v[166:169], v[92:95], v[48:63]
	ds_read_b64_tr_b16 v[166:167], v179 offset:26624
	ds_read_b64_tr_b16 v[168:169], v179 offset:27136
	s_waitcnt lgkmcnt(4)
	v_mfma_f32_32x32x16_bf16 v[32:47], v[104:107], v[88:91], v[32:47]
	ds_read_b64_tr_b16 v[104:105], v179 offset:27648
	ds_read_b64_tr_b16 v[106:107], v179 offset:28160
	s_waitcnt lgkmcnt(4)
	v_mfma_f32_32x32x16_bf16 v[32:47], v[108:111], v[84:87], v[32:47]
	ds_read_b64_tr_b16 v[108:109], v179 offset:28672
	ds_read_b64_tr_b16 v[110:111], v179 offset:29184
	s_waitcnt lgkmcnt(4)
	v_mfma_f32_32x32x16_bf16 v[32:47], v[166:169], v[100:103], v[32:47]
	ds_read_b64_tr_b16 v[166:167], v179 offset:29696
	ds_read_b64_tr_b16 v[168:169], v179 offset:30208
	s_waitcnt lgkmcnt(4)
	v_mfma_f32_32x32x16_bf16 v[32:47], v[104:107], v[92:95], v[32:47]
	v_add_f32_e32 v104, 0, v172
	v_add_f32_e32 v172, v174, v104
	ds_read_b64_tr_b16 v[104:105], v179 offset:30720
	ds_read_b64_tr_b16 v[106:107], v179 offset:31232
	s_waitcnt lgkmcnt(4)
	v_mfma_f32_32x32x16_bf16 v[16:31], v[108:111], v[88:91], v[16:31]
	v_add_f32_e32 v88, v176, v172
	v_add_f32_e32 v89, v177, v0
	v_add_f32_e32 v88, v178, v88
	v_add_f32_e64 v88, v96, v88
	v_add_f32_e64 v89, v97, v89
	ds_read_b64_tr_b16 v[90:91], v179 offset:32256
	v_pk_add_f32 v[96:97], v[98:99], v[88:89]
	ds_read_b64_tr_b16 v[88:89], v179 offset:31744
	s_waitcnt lgkmcnt(4)
	v_mfma_f32_32x32x16_bf16 v[16:31], v[166:169], v[84:87], v[16:31]
	v_add_f32_e64 v2, v2, v96
	v_add_f32_e64 v3, v3, v97
	v_add_f32_e64 v2, v6, v2
	v_add_f32_e64 v3, v7, v3
	v_add_f32_e64 v2, v10, v2
	v_add_f32_e64 v3, v11, v3
	s_waitcnt lgkmcnt(2)
	v_mfma_f32_32x32x16_bf16 v[16:31], v[104:107], v[100:103], v[16:31]
	v_add_f32_e64 v2, v12, v2
	v_add_f32_e64 v3, v13, v3
	v_add_f32_e64 v2, v14, v2
	v_add_f32_e64 v3, v15, v3
	v_add_f32_e64 v2, v80, v2
	v_add_f32_e64 v3, v81, v3
	v_pk_add_f32 v[2:3], v[82:83], v[2:3]
	s_waitcnt lgkmcnt(0)
	v_mfma_f32_32x32x16_bf16 v[16:31], v[88:91], v[92:95], v[16:31]
	v_add_f32_e64 v2, v4, v2
	v_add_f32_e64 v3, v5, v3
	v_add_f32_e64 v2, v8, v2
	v_add_f32_e64 v3, v9, v3
	v_add_f32_e64 v2, v170, v2
	v_add_f32_e64 v3, v171, v3
	v_add_f32_e32 v0, v2, v3
	v_add_f32_e32 v164, v164, v0
	s_cbranch_scc1 .LBB0_3772
	s_mov_b32 s9, s3
	s_branch .LBB0_3758

.LBB0_4953:
	v_exp_f32_e32 v176, v85
	v_exp_f32_e32 v85, v88
	v_exp_f32_e32 v88, v74
	v_add_u32_e32 v74, s18, v150
	v_add3_u32 v178, v74, v151, v130
	v_exp_f32_e32 v139, v66
	v_exp_f32_e32 v174, v84
	v_exp_f32_e32 v175, v68
	v_exp_f32_e32 v66, v70
	v_exp_f32_e32 v84, v72
	v_exp_f32_e32 v146, v76
	v_exp_f32_e32 v68, v77
	v_exp_f32_e32 v70, v78
	v_exp_f32_e32 v72, v79
	ds_read_b64_tr_b16 v[76:77], v178 offset:16384
	ds_read_b64_tr_b16 v[78:79], v178 offset:16896
	v_exp_f32_e32 v137, v82
	v_exp_f32_e32 v172, v83
	v_exp_f32_e32 v173, v67
	v_exp_f32_e32 v67, v86
	v_exp_f32_e32 v83, v87
	v_exp_f32_e32 v87, v89
	v_exp_f32_e32 v177, v69
	v_exp_f32_e32 v82, v71
	v_exp_f32_e32 v86, v73
	v_exp_f32_e32 v147, v92
	v_exp_f32_e32 v69, v93
	v_exp_f32_e32 v71, v94
	v_exp_f32_e32 v73, v95
	v_cvt_pk_bf16_f32 v92, v137, v172
	v_cvt_pk_bf16_f32 v93, v174, v176
	v_cvt_pk_bf16_f32 v94, v67, v83
	v_cvt_pk_bf16_f32 v95, v85, v87
	ds_read_b64_tr_b16 v[152:153], v178 offset:17408
	ds_read_b64_tr_b16 v[154:155], v178 offset:17920
	ds_read_b64_tr_b16 v[156:157], v178 offset:18432
	ds_read_b64_tr_b16 v[158:159], v178 offset:18944
	s_waitcnt lgkmcnt(4)
	v_mfma_f32_32x32x16_bf16 v[50:65], v[76:79], v[92:95], v[50:65]
	v_exp_f32_e32 v89, v90
	v_exp_f32_e32 v91, v91
	v_exp_f32_e32 v90, v75
	v_exp_f32_e32 v75, v96
	v_exp_f32_e32 v97, v97
	v_cvt_pk_bf16_f32 v76, v89, v91
	v_cvt_pk_bf16_f32 v77, v147, v69
	v_cvt_pk_bf16_f32 v78, v71, v73
	v_cvt_pk_bf16_f32 v79, v75, v97
	ds_read_b64_tr_b16 v[160:161], v178 offset:19456
	ds_read_b64_tr_b16 v[162:163], v178 offset:19968
	s_waitcnt lgkmcnt(4)
	v_mfma_f32_32x32x16_bf16 v[50:65], v[152:155], v[76:79], v[50:65]
	v_cvt_pk_bf16_f32 v152, v139, v173
	v_cvt_pk_bf16_f32 v153, v175, v177
	v_cvt_pk_bf16_f32 v154, v66, v82
	v_cvt_pk_bf16_f32 v155, v84, v86
	ds_read_b64_tr_b16 v[164:165], v178 offset:20480
	ds_read_b64_tr_b16 v[166:167], v178 offset:20992
	v_exp_f32_e32 v74, v80
	s_waitcnt lgkmcnt(4)
	v_mfma_f32_32x32x16_bf16 v[50:65], v[156:159], v[152:155], v[50:65]
	v_exp_f32_e32 v96, v81
	v_cvt_pk_bf16_f32 v156, v88, v90
	v_cvt_pk_bf16_f32 v157, v146, v68
	v_cvt_pk_bf16_f32 v158, v70, v72
	v_cvt_pk_bf16_f32 v159, v74, v96
	ds_read_b64_tr_b16 v[168:169], v178 offset:21504
	ds_read_b64_tr_b16 v[170:171], v178 offset:22016
	s_waitcnt lgkmcnt(4)
	v_mfma_f32_32x32x16_bf16 v[50:65], v[160:163], v[156:159], v[50:65]
	ds_read_b64_tr_b16 v[160:161], v178 offset:22528
	ds_read_b64_tr_b16 v[162:163], v178 offset:23040
	v_add_f32_e32 v80, 0, v137
	v_add_f32_e32 v81, 0, v139
	v_add_f32_e32 v80, v172, v80
	v_add_f32_e32 v81, v173, v81
	v_add_f32_e32 v80, v174, v80
	s_waitcnt lgkmcnt(4)
	v_mfma_f32_32x32x16_bf16 v[34:49], v[164:167], v[92:95], v[34:49]
	ds_read_b64_tr_b16 v[164:165], v178 offset:23552
	ds_read_b64_tr_b16 v[166:167], v178 offset:24064
	s_andn2_b64 vcc, exec, s[16:17]
	s_xor_b32 s15, s15, 1
	s_waitcnt lgkmcnt(4)
	v_mfma_f32_32x32x16_bf16 v[34:49], v[168:171], v[76:79], v[34:49]
	ds_read_b64_tr_b16 v[168:169], v178 offset:24576
	ds_read_b64_tr_b16 v[170:171], v178 offset:25088
	s_waitcnt lgkmcnt(4)
	v_mfma_f32_32x32x16_bf16 v[34:49], v[160:163], v[152:155], v[34:49]
	ds_read_b64_tr_b16 v[160:161], v178 offset:25600
	ds_read_b64_tr_b16 v[162:163], v178 offset:26112
	s_waitcnt lgkmcnt(4)
	v_mfma_f32_32x32x16_bf16 v[34:49], v[164:167], v[156:159], v[34:49]
	ds_read_b64_tr_b16 v[164:165], v178 offset:26624
	ds_read_b64_tr_b16 v[166:167], v178 offset:27136
	s_waitcnt lgkmcnt(4)
	v_mfma_f32_32x32x16_bf16 v[18:33], v[168:171], v[92:95], v[18:33]
	ds_read_b64_tr_b16 v[168:169], v178 offset:27648
	ds_read_b64_tr_b16 v[170:171], v178 offset:28160
	s_waitcnt lgkmcnt(4)
	v_mfma_f32_32x32x16_bf16 v[18:33], v[160:163], v[76:79], v[18:33]
	ds_read_b64_tr_b16 v[160:161], v178 offset:28672
	ds_read_b64_tr_b16 v[162:163], v178 offset:29184
	s_waitcnt lgkmcnt(4)
	v_mfma_f32_32x32x16_bf16 v[18:33], v[164:167], v[152:155], v[18:33]
	ds_read_b64_tr_b16 v[164:165], v178 offset:29696
	ds_read_b64_tr_b16 v[166:167], v178 offset:30208
	s_waitcnt lgkmcnt(4)
	v_mfma_f32_32x32x16_bf16 v[18:33], v[168:171], v[156:159], v[18:33]
	ds_read_b64_tr_b16 v[168:169], v178 offset:30720
	ds_read_b64_tr_b16 v[170:171], v178 offset:31232
	s_waitcnt lgkmcnt(4)
	v_mfma_f32_32x32x16_bf16 v[2:17], v[160:163], v[92:95], v[2:17]
	v_add_f32_e32 v92, v175, v81
	v_add_f32_e32 v81, v176, v80
	v_add_f32_e32 v80, v177, v92
	ds_read_b64_tr_b16 v[92:93], v178 offset:31744
	ds_read_b64_tr_b16 v[94:95], v178 offset:32256
	v_pk_add_f32 v[66:67], v[66:67], v[80:81]
	s_waitcnt lgkmcnt(4)
	v_mfma_f32_32x32x16_bf16 v[2:17], v[164:167], v[76:79], v[2:17]
	v_add_f32_e64 v66, v82, v66
	v_add_f32_e64 v67, v83, v67
	v_add_f32_e64 v66, v84, v66
	v_add_f32_e64 v67, v85, v67
	v_add_f32_e64 v66, v86, v66
	v_add_f32_e64 v67, v87, v67
	v_pk_add_f32 v[66:67], v[88:89], v[66:67]
	s_waitcnt lgkmcnt(2)
	v_mfma_f32_32x32x16_bf16 v[2:17], v[168:171], v[152:155], v[2:17]
	v_add_f32_e64 v66, v90, v66
	v_add_f32_e64 v67, v91, v67
	v_add_f32_e64 v66, v146, v66
	v_add_f32_e64 v67, v147, v67
	v_add_f32_e64 v66, v68, v66
	v_add_f32_e64 v67, v69, v67
	v_pk_add_f32 v[66:67], v[70:71], v[66:67]
	s_waitcnt lgkmcnt(0)
	v_mfma_f32_32x32x16_bf16 v[2:17], v[92:95], v[156:159], v[2:17]
	v_add_f32_e64 v66, v72, v66
	v_add_f32_e64 v67, v73, v67
	v_add_f32_e64 v66, v74, v66
	v_add_f32_e64 v67, v75, v67
	v_add_f32_e64 v66, v96, v66
	v_add_f32_e64 v67, v97, v67
	v_add_f32_e32 v66, v66, v67
	v_add_f32_e32 v133, v133, v66
	s_cbranch_vccz .LBB0_4951
